# speedup vs baseline: 1.0237x; 1.0037x over previous
.Lk_first:
	ds_read_b128 v[130:133], v219 offset:32768
	ds_read_b128 v[134:137], v219 offset:33792
	ds_read_b128 v[138:141], v219 offset:34816
	ds_read_b128 v[142:145], v219 offset:35840
	ds_read_b128 v[178:181], v219 offset:49152
	ds_read_b128 v[182:185], v219 offset:50176
	ds_read_b128 v[186:189], v219 offset:51200
	ds_read_b128 v[190:193], v219 offset:52224
	ds_read_b128 v[146:149], v220
	ds_read_b128 v[150:153], v220 offset:1024
	ds_read_b128 v[154:157], v221
	ds_read_b128 v[158:161], v221 offset:1024
	ds_read_b128 v[162:165], v222
	ds_read_b128 v[166:169], v222 offset:1024
	ds_read_b128 v[170:173], v223
	ds_read_b128 v[174:177], v223 offset:1024
	s_add_i32 s12, s8, 1
	s_mov_b32 m0, s43
	v_readlane_b32 s9, v248, s12
	s_nop 1
	v_add_u32_e32 v251, s9, v249
	global_load_lds_dwordx4 v251, s[18:19]
	v_add_u32_e32 v251, s9, v250
	s_mov_b32 m0, s44
	s_nop 0
	global_load_lds_dwordx4 v251, s[18:19]
	s_waitcnt lgkmcnt(0)
	s_barrier
	s_setprio 1
	v_mfma_f32_16x16x32_f16 v[124:127], v[130:133], v[146:149], 0
	v_mfma_f32_16x16x32_f16 v[124:127], v[134:137], v[150:153], v[124:127]
	v_mfma_f32_16x16x32_f16 v[120:123], v[138:141], v[146:149], 0
	v_mfma_f32_16x16x32_f16 v[120:123], v[142:145], v[150:153], v[120:123]
	v_mfma_f32_16x16x32_f16 v[52:55], v[178:181], v[146:149], 0
	v_mfma_f32_16x16x32_f16 v[52:55], v[182:185], v[150:153], v[52:55]
	v_mfma_f32_16x16x32_f16 v[40:43], v[186:189], v[146:149], 0
	v_mfma_f32_16x16x32_f16 v[40:43], v[190:193], v[150:153], v[40:43]
	v_mfma_f32_16x16x32_f16 v[32:35], v[186:189], v[154:157], 0
	v_mfma_f32_16x16x32_f16 v[32:35], v[190:193], v[158:161], v[32:35]
	v_mfma_f32_16x16x32_f16 v[36:39], v[178:181], v[154:157], 0
	v_mfma_f32_16x16x32_f16 v[36:39], v[182:185], v[158:161], v[36:39]
	v_mfma_f32_16x16x32_f16 v[112:115], v[138:141], v[154:157], 0
	v_mfma_f32_16x16x32_f16 v[112:115], v[142:145], v[158:161], v[112:115]
	v_mfma_f32_16x16x32_f16 v[116:119], v[130:133], v[154:157], 0
	v_mfma_f32_16x16x32_f16 v[116:119], v[134:137], v[158:161], v[116:119]
	v_mfma_f32_16x16x32_f16 v[108:111], v[130:133], v[162:165], 0
	v_mfma_f32_16x16x32_f16 v[108:111], v[134:137], v[166:169], v[108:111]
	v_mfma_f32_16x16x32_f16 v[104:107], v[138:141], v[162:165], 0
	v_mfma_f32_16x16x32_f16 v[104:107], v[142:145], v[166:169], v[104:107]
	v_mfma_f32_16x16x32_f16 v[28:31], v[178:181], v[162:165], 0
	v_mfma_f32_16x16x32_f16 v[28:31], v[182:185], v[166:169], v[28:31]
	v_mfma_f32_16x16x32_f16 v[24:27], v[186:189], v[162:165], 0
	v_mfma_f32_16x16x32_f16 v[24:27], v[190:193], v[166:169], v[24:27]
	v_mfma_f32_16x16x32_f16 v[16:19], v[186:189], v[170:173], 0
	v_mfma_f32_16x16x32_f16 v[16:19], v[190:193], v[174:177], v[16:19]
	v_mfma_f32_16x16x32_f16 v[20:23], v[178:181], v[170:173], 0
	v_mfma_f32_16x16x32_f16 v[20:23], v[182:185], v[174:177], v[20:23]
	v_mfma_f32_16x16x32_f16 v[96:99], v[138:141], v[170:173], 0
	v_mfma_f32_16x16x32_f16 v[96:99], v[142:145], v[174:177], v[96:99]
	v_mfma_f32_16x16x32_f16 v[100:103], v[130:133], v[170:173], 0
	v_mfma_f32_16x16x32_f16 v[100:103], v[134:137], v[174:177], v[100:103]
	s_setprio 0
	s_barrier
	ds_read_b128 v[146:149], v220 offset:16384
	ds_read_b128 v[150:153], v220 offset:17408
	ds_read_b128 v[154:157], v221 offset:16384
	ds_read_b128 v[158:161], v221 offset:17408
	ds_read_b128 v[162:165], v222 offset:16384
	ds_read_b128 v[166:169], v222 offset:17408
	ds_read_b128 v[170:173], v223 offset:16384
	ds_read_b128 v[174:177], v223 offset:17408
	v_add_u32_e32 v129, s7, v128
	s_mov_b32 m0, s22
	v_add_u32_e32 v194, 0xffffff80, v129
	global_load_lds_dwordx4 v194, s[10:11]
	v_add_u32_e32 v194, 0x47f80, v129
	s_mov_b32 m0, s23
	s_add_i32 s9, s8, 2
	global_load_lds_dwordx4 v194, s[10:11]
	v_readlane_b32 s13, v248, s9
	s_mov_b32 m0, s21
	s_nop 1
	v_add_u32_e32 v194, s13, v206
	global_load_lds_dwordx4 v194, s[18:19]
	v_add_u32_e32 v194, s13, v213
	s_mov_b32 m0, s24
	s_nop 0
	global_load_lds_dwordx4 v194, s[18:19]
	s_mov_b32 m0, s25
	v_add_u32_e32 v194, 0x8ff80, v129
	global_load_lds_dwordx4 v194, s[10:11]
	v_add_u32_e32 v194, 0xd7f80, v129
	s_mov_b32 m0, s26
	s_nop 0
	global_load_lds_dwordx4 v194, s[10:11]
	s_waitcnt vmcnt(8) lgkmcnt(0)
	s_barrier
	s_setprio 1
	v_mfma_f32_16x16x32_f16 v[12:15], v[130:133], v[146:149], 0
	v_mfma_f32_16x16x32_f16 v[12:15], v[134:137], v[150:153], v[12:15]
	v_mfma_f32_16x16x32_f16 v[8:11], v[138:141], v[146:149], 0
	v_mfma_f32_16x16x32_f16 v[8:11], v[142:145], v[150:153], v[8:11]
	v_mfma_f32_16x16x32_f16 v[64:67], v[178:181], v[146:149], 0
	v_mfma_f32_16x16x32_f16 v[64:67], v[182:185], v[150:153], v[64:67]
	v_mfma_f32_16x16x32_f16 v[68:71], v[186:189], v[146:149], 0
	v_mfma_f32_16x16x32_f16 v[68:71], v[190:193], v[150:153], v[68:71]
	v_mfma_f32_16x16x32_f16 v[76:79], v[186:189], v[154:157], 0
	v_mfma_f32_16x16x32_f16 v[76:79], v[190:193], v[158:161], v[76:79]
	v_mfma_f32_16x16x32_f16 v[72:75], v[178:181], v[154:157], 0
	v_mfma_f32_16x16x32_f16 v[72:75], v[182:185], v[158:161], v[72:75]
	v_mfma_f32_16x16x32_f16 v[0:3], v[138:141], v[154:157], 0
	v_mfma_f32_16x16x32_f16 v[0:3], v[142:145], v[158:161], v[0:3]
	v_mfma_f32_16x16x32_f16 v[4:7], v[130:133], v[154:157], 0
	v_mfma_f32_16x16x32_f16 v[4:7], v[134:137], v[158:161], v[4:7]
	v_mfma_f32_16x16x32_f16 v[44:47], v[130:133], v[162:165], 0
	v_mfma_f32_16x16x32_f16 v[44:47], v[134:137], v[166:169], v[44:47]
	v_mfma_f32_16x16x32_f16 v[48:51], v[138:141], v[162:165], 0
	v_mfma_f32_16x16x32_f16 v[48:51], v[142:145], v[166:169], v[48:51]
	v_mfma_f32_16x16x32_f16 v[80:83], v[178:181], v[162:165], 0
	v_mfma_f32_16x16x32_f16 v[80:83], v[182:185], v[166:169], v[80:83]
	v_mfma_f32_16x16x32_f16 v[84:87], v[186:189], v[162:165], 0
	v_mfma_f32_16x16x32_f16 v[84:87], v[190:193], v[166:169], v[84:87]
	v_mfma_f32_16x16x32_f16 v[92:95], v[186:189], v[170:173], 0
	v_mfma_f32_16x16x32_f16 v[92:95], v[190:193], v[174:177], v[92:95]
	v_mfma_f32_16x16x32_f16 v[88:91], v[178:181], v[170:173], 0
	v_mfma_f32_16x16x32_f16 v[88:91], v[182:185], v[174:177], v[88:91]
	v_mfma_f32_16x16x32_f16 v[60:63], v[138:141], v[170:173], 0
	v_mfma_f32_16x16x32_f16 v[60:63], v[142:145], v[174:177], v[60:63]
	v_mfma_f32_16x16x32_f16 v[56:59], v[130:133], v[170:173], 0
	v_mfma_f32_16x16x32_f16 v[56:59], v[134:137], v[174:177], v[56:59]
	s_setprio 0
	s_barrier
	ds_read_b128 v[130:133], v224
	ds_read_b128 v[134:137], v224 offset:1024
	ds_read_b128 v[138:141], v224 offset:2048
	ds_read_b128 v[142:145], v224 offset:3072
	ds_read_b128 v[178:181], v229
	ds_read_b128 v[182:185], v229 offset:1024
	ds_read_b128 v[186:189], v229 offset:2048
	ds_read_b128 v[190:193], v229 offset:3072
	ds_read_b128 v[146:149], v225
	ds_read_b128 v[150:153], v225 offset:1024
	ds_read_b128 v[154:157], v226
	ds_read_b128 v[158:161], v226 offset:1024
	ds_read_b128 v[162:165], v227
	ds_read_b128 v[166:169], v227 offset:1024
	ds_read_b128 v[170:173], v228
	ds_read_b128 v[174:177], v228 offset:1024
	v_readlane_b32 s12, v248, s9
	s_mov_b32 m0, s27
	s_nop 1
	v_add_u32_e32 v251, s12, v249
	global_load_lds_dwordx4 v251, s[18:19]
	v_add_u32_e32 v251, s12, v250
	s_mov_b32 m0, s28
	s_nop 0
	global_load_lds_dwordx4 v251, s[18:19]
	s_waitcnt vmcnt(8) lgkmcnt(0)
	s_barrier
	s_setprio 1
	v_mfma_f32_16x16x32_f16 v[124:127], v[130:133], v[146:149], v[124:127]
	v_mfma_f32_16x16x32_f16 v[124:127], v[134:137], v[150:153], v[124:127]
	v_mfma_f32_16x16x32_f16 v[120:123], v[138:141], v[146:149], v[120:123]
	v_mfma_f32_16x16x32_f16 v[120:123], v[142:145], v[150:153], v[120:123]
	v_mfma_f32_16x16x32_f16 v[52:55], v[178:181], v[146:149], v[52:55]
	v_mfma_f32_16x16x32_f16 v[52:55], v[182:185], v[150:153], v[52:55]
	v_mfma_f32_16x16x32_f16 v[40:43], v[186:189], v[146:149], v[40:43]
	v_mfma_f32_16x16x32_f16 v[40:43], v[190:193], v[150:153], v[40:43]
	v_mfma_f32_16x16x32_f16 v[32:35], v[186:189], v[154:157], v[32:35]
	v_mfma_f32_16x16x32_f16 v[32:35], v[190:193], v[158:161], v[32:35]
	v_mfma_f32_16x16x32_f16 v[36:39], v[178:181], v[154:157], v[36:39]
	v_mfma_f32_16x16x32_f16 v[36:39], v[182:185], v[158:161], v[36:39]
	v_mfma_f32_16x16x32_f16 v[112:115], v[138:141], v[154:157], v[112:115]
	v_mfma_f32_16x16x32_f16 v[112:115], v[142:145], v[158:161], v[112:115]
	v_mfma_f32_16x16x32_f16 v[116:119], v[130:133], v[154:157], v[116:119]
	v_mfma_f32_16x16x32_f16 v[116:119], v[134:137], v[158:161], v[116:119]
	v_mfma_f32_16x16x32_f16 v[108:111], v[130:133], v[162:165], v[108:111]
	v_mfma_f32_16x16x32_f16 v[108:111], v[134:137], v[166:169], v[108:111]
	v_mfma_f32_16x16x32_f16 v[104:107], v[138:141], v[162:165], v[104:107]
	v_mfma_f32_16x16x32_f16 v[104:107], v[142:145], v[166:169], v[104:107]
	v_mfma_f32_16x16x32_f16 v[28:31], v[178:181], v[162:165], v[28:31]
	v_mfma_f32_16x16x32_f16 v[28:31], v[182:185], v[166:169], v[28:31]
	v_mfma_f32_16x16x32_f16 v[24:27], v[186:189], v[162:165], v[24:27]
	v_mfma_f32_16x16x32_f16 v[24:27], v[190:193], v[166:169], v[24:27]
	v_mfma_f32_16x16x32_f16 v[16:19], v[186:189], v[170:173], v[16:19]
	v_mfma_f32_16x16x32_f16 v[16:19], v[190:193], v[174:177], v[16:19]
	v_mfma_f32_16x16x32_f16 v[20:23], v[178:181], v[170:173], v[20:23]
	v_mfma_f32_16x16x32_f16 v[20:23], v[182:185], v[174:177], v[20:23]
	v_mfma_f32_16x16x32_f16 v[96:99], v[138:141], v[170:173], v[96:99]
	v_mfma_f32_16x16x32_f16 v[96:99], v[142:145], v[174:177], v[96:99]
	v_mfma_f32_16x16x32_f16 v[100:103], v[130:133], v[170:173], v[100:103]
	v_mfma_f32_16x16x32_f16 v[100:103], v[134:137], v[174:177], v[100:103]
	s_setprio 0
	s_barrier
	ds_read_b128 v[146:149], v230
	ds_read_b128 v[150:153], v230 offset:1024
	ds_read_b128 v[154:157], v231
	ds_read_b128 v[158:161], v231 offset:1024
	ds_read_b128 v[162:165], v232
	ds_read_b128 v[166:169], v232 offset:1024
	ds_read_b128 v[170:173], v233
	ds_read_b128 v[174:177], v233 offset:1024
	s_mov_b32 m0, s37
	v_add_u32_e32 v194, 0x48000, v129
	global_load_lds_dwordx4 v129, s[10:11]
	s_mov_b32 m0, s38
	s_add_i32 s12, s8, 3
	global_load_lds_dwordx4 v194, s[10:11]
	v_readlane_b32 s13, v248, s12
	s_mov_b32 m0, s39
	s_nop 1
	v_add_u32_e32 v194, s13, v206
	global_load_lds_dwordx4 v194, s[18:19]
	v_add_u32_e32 v194, s13, v213
	s_mov_b32 m0, s40
	s_nop 0
	global_load_lds_dwordx4 v194, s[18:19]
	s_mov_b32 m0, s41
	v_add_u32_e32 v194, 0x90000, v129
	global_load_lds_dwordx4 v194, s[10:11]
	v_add_u32_e32 v194, 0xd8000, v129
	s_mov_b32 m0, s42
	s_nop 0
	global_load_lds_dwordx4 v194, s[10:11]
	s_waitcnt vmcnt(8) lgkmcnt(0)
	s_barrier
	s_setprio 1
	v_mfma_f32_16x16x32_f16 v[12:15], v[130:133], v[146:149], v[12:15]
	v_mfma_f32_16x16x32_f16 v[12:15], v[134:137], v[150:153], v[12:15]
	v_mfma_f32_16x16x32_f16 v[8:11], v[138:141], v[146:149], v[8:11]
	v_mfma_f32_16x16x32_f16 v[8:11], v[142:145], v[150:153], v[8:11]
	v_mfma_f32_16x16x32_f16 v[64:67], v[178:181], v[146:149], v[64:67]
	v_mfma_f32_16x16x32_f16 v[64:67], v[182:185], v[150:153], v[64:67]
	v_mfma_f32_16x16x32_f16 v[68:71], v[186:189], v[146:149], v[68:71]
	v_mfma_f32_16x16x32_f16 v[68:71], v[190:193], v[150:153], v[68:71]
	v_mfma_f32_16x16x32_f16 v[76:79], v[186:189], v[154:157], v[76:79]
	v_mfma_f32_16x16x32_f16 v[76:79], v[190:193], v[158:161], v[76:79]
	v_mfma_f32_16x16x32_f16 v[72:75], v[178:181], v[154:157], v[72:75]
	v_mfma_f32_16x16x32_f16 v[72:75], v[182:185], v[158:161], v[72:75]
	v_mfma_f32_16x16x32_f16 v[0:3], v[138:141], v[154:157], v[0:3]
	v_mfma_f32_16x16x32_f16 v[0:3], v[142:145], v[158:161], v[0:3]
	v_mfma_f32_16x16x32_f16 v[4:7], v[130:133], v[154:157], v[4:7]
	v_mfma_f32_16x16x32_f16 v[4:7], v[134:137], v[158:161], v[4:7]
	v_mfma_f32_16x16x32_f16 v[44:47], v[130:133], v[162:165], v[44:47]
	v_mfma_f32_16x16x32_f16 v[44:47], v[134:137], v[166:169], v[44:47]
	v_mfma_f32_16x16x32_f16 v[48:51], v[138:141], v[162:165], v[48:51]
	v_mfma_f32_16x16x32_f16 v[48:51], v[142:145], v[166:169], v[48:51]
	v_mfma_f32_16x16x32_f16 v[80:83], v[178:181], v[162:165], v[80:83]
	v_mfma_f32_16x16x32_f16 v[80:83], v[182:185], v[166:169], v[80:83]
	v_mfma_f32_16x16x32_f16 v[84:87], v[186:189], v[162:165], v[84:87]
	v_mfma_f32_16x16x32_f16 v[84:87], v[190:193], v[166:169], v[84:87]
	v_mfma_f32_16x16x32_f16 v[92:95], v[186:189], v[170:173], v[92:95]
	v_mfma_f32_16x16x32_f16 v[92:95], v[190:193], v[174:177], v[92:95]
	v_mfma_f32_16x16x32_f16 v[88:91], v[178:181], v[170:173], v[88:91]
	v_mfma_f32_16x16x32_f16 v[88:91], v[182:185], v[174:177], v[88:91]
	v_mfma_f32_16x16x32_f16 v[60:63], v[138:141], v[170:173], v[60:63]
	v_mfma_f32_16x16x32_f16 v[60:63], v[142:145], v[174:177], v[60:63]
	v_mfma_f32_16x16x32_f16 v[56:59], v[130:133], v[170:173], v[56:59]
	v_mfma_f32_16x16x32_f16 v[56:59], v[134:137], v[174:177], v[56:59]
	s_setprio 0
	s_addk_i32 s7, 0x100
	s_cmp_lt_u32 s8, 32
	s_mov_b32 s8, s9
	s_barrier
.LBB1_82:
	ds_read_b128 v[130:133], v219 offset:32768
	ds_read_b128 v[134:137], v219 offset:33792
	ds_read_b128 v[138:141], v219 offset:34816
	ds_read_b128 v[142:145], v219 offset:35840
	ds_read_b128 v[178:181], v219 offset:49152
	ds_read_b128 v[182:185], v219 offset:50176
	ds_read_b128 v[186:189], v219 offset:51200
	ds_read_b128 v[190:193], v219 offset:52224
	ds_read_b128 v[146:149], v220
	ds_read_b128 v[150:153], v220 offset:1024
	ds_read_b128 v[154:157], v221
	ds_read_b128 v[158:161], v221 offset:1024
	ds_read_b128 v[162:165], v222
	ds_read_b128 v[166:169], v222 offset:1024
	ds_read_b128 v[170:173], v223
	ds_read_b128 v[174:177], v223 offset:1024
	s_add_i32 s12, s8, 1
	s_mov_b32 m0, s43
	v_readlane_b32 s9, v248, s12
	s_nop 1
	v_add_u32_e32 v251, s9, v249
	global_load_lds_dwordx4 v251, s[18:19]
	v_add_u32_e32 v251, s9, v250
	s_mov_b32 m0, s44
	s_nop 0
	global_load_lds_dwordx4 v251, s[18:19]
	s_waitcnt vmcnt(8) lgkmcnt(0)
	s_barrier
	s_setprio 1
	v_mfma_f32_16x16x32_f16 v[124:127], v[130:133], v[146:149], v[124:127]
	v_mfma_f32_16x16x32_f16 v[124:127], v[134:137], v[150:153], v[124:127]
	v_mfma_f32_16x16x32_f16 v[120:123], v[138:141], v[146:149], v[120:123]
	v_mfma_f32_16x16x32_f16 v[120:123], v[142:145], v[150:153], v[120:123]
	v_mfma_f32_16x16x32_f16 v[52:55], v[178:181], v[146:149], v[52:55]
	v_mfma_f32_16x16x32_f16 v[52:55], v[182:185], v[150:153], v[52:55]
	v_mfma_f32_16x16x32_f16 v[40:43], v[186:189], v[146:149], v[40:43]
	v_mfma_f32_16x16x32_f16 v[40:43], v[190:193], v[150:153], v[40:43]
	v_mfma_f32_16x16x32_f16 v[32:35], v[186:189], v[154:157], v[32:35]
	v_mfma_f32_16x16x32_f16 v[32:35], v[190:193], v[158:161], v[32:35]
	v_mfma_f32_16x16x32_f16 v[36:39], v[178:181], v[154:157], v[36:39]
	v_mfma_f32_16x16x32_f16 v[36:39], v[182:185], v[158:161], v[36:39]
	v_mfma_f32_16x16x32_f16 v[112:115], v[138:141], v[154:157], v[112:115]
	v_mfma_f32_16x16x32_f16 v[112:115], v[142:145], v[158:161], v[112:115]
	v_mfma_f32_16x16x32_f16 v[116:119], v[130:133], v[154:157], v[116:119]
	v_mfma_f32_16x16x32_f16 v[116:119], v[134:137], v[158:161], v[116:119]
	v_mfma_f32_16x16x32_f16 v[108:111], v[130:133], v[162:165], v[108:111]
	v_mfma_f32_16x16x32_f16 v[108:111], v[134:137], v[166:169], v[108:111]
	v_mfma_f32_16x16x32_f16 v[104:107], v[138:141], v[162:165], v[104:107]
	v_mfma_f32_16x16x32_f16 v[104:107], v[142:145], v[166:169], v[104:107]
	v_mfma_f32_16x16x32_f16 v[28:31], v[178:181], v[162:165], v[28:31]
	v_mfma_f32_16x16x32_f16 v[28:31], v[182:185], v[166:169], v[28:31]
	v_mfma_f32_16x16x32_f16 v[24:27], v[186:189], v[162:165], v[24:27]
	v_mfma_f32_16x16x32_f16 v[24:27], v[190:193], v[166:169], v[24:27]
	v_mfma_f32_16x16x32_f16 v[16:19], v[186:189], v[170:173], v[16:19]
	v_mfma_f32_16x16x32_f16 v[16:19], v[190:193], v[174:177], v[16:19]
	v_mfma_f32_16x16x32_f16 v[20:23], v[178:181], v[170:173], v[20:23]
	v_mfma_f32_16x16x32_f16 v[20:23], v[182:185], v[174:177], v[20:23]
	v_mfma_f32_16x16x32_f16 v[96:99], v[138:141], v[170:173], v[96:99]
	v_mfma_f32_16x16x32_f16 v[96:99], v[142:145], v[174:177], v[96:99]
	v_mfma_f32_16x16x32_f16 v[100:103], v[130:133], v[170:173], v[100:103]
	v_mfma_f32_16x16x32_f16 v[100:103], v[134:137], v[174:177], v[100:103]
	s_setprio 0
	s_barrier
	ds_read_b128 v[146:149], v220 offset:16384
	ds_read_b128 v[150:153], v220 offset:17408
	ds_read_b128 v[154:157], v221 offset:16384
	ds_read_b128 v[158:161], v221 offset:17408
	ds_read_b128 v[162:165], v222 offset:16384
	ds_read_b128 v[166:169], v222 offset:17408
	ds_read_b128 v[170:173], v223 offset:16384
	ds_read_b128 v[174:177], v223 offset:17408
	v_add_u32_e32 v129, s7, v128
	s_mov_b32 m0, s22
	v_add_u32_e32 v194, 0xffffff80, v129
	global_load_lds_dwordx4 v194, s[10:11]
	v_add_u32_e32 v194, 0x47f80, v129
	s_mov_b32 m0, s23
	s_add_i32 s9, s8, 2
	global_load_lds_dwordx4 v194, s[10:11]
	v_readlane_b32 s13, v248, s9
	s_mov_b32 m0, s21
	s_nop 1
	v_add_u32_e32 v194, s13, v206
	global_load_lds_dwordx4 v194, s[18:19]
	v_add_u32_e32 v194, s13, v213
	s_mov_b32 m0, s24
	s_nop 0
	global_load_lds_dwordx4 v194, s[18:19]
	s_mov_b32 m0, s25
	v_add_u32_e32 v194, 0x8ff80, v129
	global_load_lds_dwordx4 v194, s[10:11]
	v_add_u32_e32 v194, 0xd7f80, v129
	s_mov_b32 m0, s26
	s_nop 0
	global_load_lds_dwordx4 v194, s[10:11]
	s_waitcnt vmcnt(8) lgkmcnt(0)
	s_barrier
	s_setprio 1
	v_mfma_f32_16x16x32_f16 v[12:15], v[130:133], v[146:149], v[12:15]
	v_mfma_f32_16x16x32_f16 v[12:15], v[134:137], v[150:153], v[12:15]
	v_mfma_f32_16x16x32_f16 v[8:11], v[138:141], v[146:149], v[8:11]
	v_mfma_f32_16x16x32_f16 v[8:11], v[142:145], v[150:153], v[8:11]
	v_mfma_f32_16x16x32_f16 v[64:67], v[178:181], v[146:149], v[64:67]
	v_mfma_f32_16x16x32_f16 v[64:67], v[182:185], v[150:153], v[64:67]
	v_mfma_f32_16x16x32_f16 v[68:71], v[186:189], v[146:149], v[68:71]
	v_mfma_f32_16x16x32_f16 v[68:71], v[190:193], v[150:153], v[68:71]
	v_mfma_f32_16x16x32_f16 v[76:79], v[186:189], v[154:157], v[76:79]
	v_mfma_f32_16x16x32_f16 v[76:79], v[190:193], v[158:161], v[76:79]
	v_mfma_f32_16x16x32_f16 v[72:75], v[178:181], v[154:157], v[72:75]
	v_mfma_f32_16x16x32_f16 v[72:75], v[182:185], v[158:161], v[72:75]
	v_mfma_f32_16x16x32_f16 v[0:3], v[138:141], v[154:157], v[0:3]
	v_mfma_f32_16x16x32_f16 v[0:3], v[142:145], v[158:161], v[0:3]
	v_mfma_f32_16x16x32_f16 v[4:7], v[130:133], v[154:157], v[4:7]
	v_mfma_f32_16x16x32_f16 v[4:7], v[134:137], v[158:161], v[4:7]
	v_mfma_f32_16x16x32_f16 v[44:47], v[130:133], v[162:165], v[44:47]
	v_mfma_f32_16x16x32_f16 v[44:47], v[134:137], v[166:169], v[44:47]
	v_mfma_f32_16x16x32_f16 v[48:51], v[138:141], v[162:165], v[48:51]
	v_mfma_f32_16x16x32_f16 v[48:51], v[142:145], v[166:169], v[48:51]
	v_mfma_f32_16x16x32_f16 v[80:83], v[178:181], v[162:165], v[80:83]
	v_mfma_f32_16x16x32_f16 v[80:83], v[182:185], v[166:169], v[80:83]
	v_mfma_f32_16x16x32_f16 v[84:87], v[186:189], v[162:165], v[84:87]
	v_mfma_f32_16x16x32_f16 v[84:87], v[190:193], v[166:169], v[84:87]
	v_mfma_f32_16x16x32_f16 v[92:95], v[186:189], v[170:173], v[92:95]
	v_mfma_f32_16x16x32_f16 v[92:95], v[190:193], v[174:177], v[92:95]
	v_mfma_f32_16x16x32_f16 v[88:91], v[178:181], v[170:173], v[88:91]
	v_mfma_f32_16x16x32_f16 v[88:91], v[182:185], v[174:177], v[88:91]
	v_mfma_f32_16x16x32_f16 v[60:63], v[138:141], v[170:173], v[60:63]
	v_mfma_f32_16x16x32_f16 v[60:63], v[142:145], v[174:177], v[60:63]
	v_mfma_f32_16x16x32_f16 v[56:59], v[130:133], v[170:173], v[56:59]
	v_mfma_f32_16x16x32_f16 v[56:59], v[134:137], v[174:177], v[56:59]
	s_setprio 0
	s_barrier
	ds_read_b128 v[130:133], v224
	ds_read_b128 v[134:137], v224 offset:1024
	ds_read_b128 v[138:141], v224 offset:2048
	ds_read_b128 v[142:145], v224 offset:3072
	ds_read_b128 v[178:181], v229
	ds_read_b128 v[182:185], v229 offset:1024
	ds_read_b128 v[186:189], v229 offset:2048
	ds_read_b128 v[190:193], v229 offset:3072
	ds_read_b128 v[146:149], v225
	ds_read_b128 v[150:153], v225 offset:1024
	ds_read_b128 v[154:157], v226
	ds_read_b128 v[158:161], v226 offset:1024
	ds_read_b128 v[162:165], v227
	ds_read_b128 v[166:169], v227 offset:1024
	ds_read_b128 v[170:173], v228
	ds_read_b128 v[174:177], v228 offset:1024
	v_readlane_b32 s12, v248, s9
	s_mov_b32 m0, s27
	s_nop 1
	v_add_u32_e32 v251, s12, v249
	global_load_lds_dwordx4 v251, s[18:19]
	v_add_u32_e32 v251, s12, v250
	s_mov_b32 m0, s28
	s_nop 0
	global_load_lds_dwordx4 v251, s[18:19]
	s_waitcnt vmcnt(8) lgkmcnt(0)
	s_barrier
	s_setprio 1
	v_mfma_f32_16x16x32_f16 v[124:127], v[130:133], v[146:149], v[124:127]
	v_mfma_f32_16x16x32_f16 v[124:127], v[134:137], v[150:153], v[124:127]
	v_mfma_f32_16x16x32_f16 v[120:123], v[138:141], v[146:149], v[120:123]
	v_mfma_f32_16x16x32_f16 v[120:123], v[142:145], v[150:153], v[120:123]
	v_mfma_f32_16x16x32_f16 v[52:55], v[178:181], v[146:149], v[52:55]
	v_mfma_f32_16x16x32_f16 v[52:55], v[182:185], v[150:153], v[52:55]
	v_mfma_f32_16x16x32_f16 v[40:43], v[186:189], v[146:149], v[40:43]
	v_mfma_f32_16x16x32_f16 v[40:43], v[190:193], v[150:153], v[40:43]
	v_mfma_f32_16x16x32_f16 v[32:35], v[186:189], v[154:157], v[32:35]
	v_mfma_f32_16x16x32_f16 v[32:35], v[190:193], v[158:161], v[32:35]
	v_mfma_f32_16x16x32_f16 v[36:39], v[178:181], v[154:157], v[36:39]
	v_mfma_f32_16x16x32_f16 v[36:39], v[182:185], v[158:161], v[36:39]
	v_mfma_f32_16x16x32_f16 v[112:115], v[138:141], v[154:157], v[112:115]
	v_mfma_f32_16x16x32_f16 v[112:115], v[142:145], v[158:161], v[112:115]
	v_mfma_f32_16x16x32_f16 v[116:119], v[130:133], v[154:157], v[116:119]
	v_mfma_f32_16x16x32_f16 v[116:119], v[134:137], v[158:161], v[116:119]
	v_mfma_f32_16x16x32_f16 v[108:111], v[130:133], v[162:165], v[108:111]
	v_mfma_f32_16x16x32_f16 v[108:111], v[134:137], v[166:169], v[108:111]
	v_mfma_f32_16x16x32_f16 v[104:107], v[138:141], v[162:165], v[104:107]
	v_mfma_f32_16x16x32_f16 v[104:107], v[142:145], v[166:169], v[104:107]
	v_mfma_f32_16x16x32_f16 v[28:31], v[178:181], v[162:165], v[28:31]
	v_mfma_f32_16x16x32_f16 v[28:31], v[182:185], v[166:169], v[28:31]
	v_mfma_f32_16x16x32_f16 v[24:27], v[186:189], v[162:165], v[24:27]
	v_mfma_f32_16x16x32_f16 v[24:27], v[190:193], v[166:169], v[24:27]
	v_mfma_f32_16x16x32_f16 v[16:19], v[186:189], v[170:173], v[16:19]
	v_mfma_f32_16x16x32_f16 v[16:19], v[190:193], v[174:177], v[16:19]
	v_mfma_f32_16x16x32_f16 v[20:23], v[178:181], v[170:173], v[20:23]
	v_mfma_f32_16x16x32_f16 v[20:23], v[182:185], v[174:177], v[20:23]
	v_mfma_f32_16x16x32_f16 v[96:99], v[138:141], v[170:173], v[96:99]
	v_mfma_f32_16x16x32_f16 v[96:99], v[142:145], v[174:177], v[96:99]
	v_mfma_f32_16x16x32_f16 v[100:103], v[130:133], v[170:173], v[100:103]
	v_mfma_f32_16x16x32_f16 v[100:103], v[134:137], v[174:177], v[100:103]
	s_setprio 0
	s_barrier
	ds_read_b128 v[146:149], v230
	ds_read_b128 v[150:153], v230 offset:1024
	ds_read_b128 v[154:157], v231
	ds_read_b128 v[158:161], v231 offset:1024
	ds_read_b128 v[162:165], v232
	ds_read_b128 v[166:169], v232 offset:1024
	ds_read_b128 v[170:173], v233
	ds_read_b128 v[174:177], v233 offset:1024
	s_mov_b32 m0, s37
	v_add_u32_e32 v194, 0x48000, v129
	global_load_lds_dwordx4 v129, s[10:11]
	s_mov_b32 m0, s38
	s_add_i32 s12, s8, 3
	global_load_lds_dwordx4 v194, s[10:11]
	v_readlane_b32 s13, v248, s12
	s_mov_b32 m0, s39
	s_nop 1
	v_add_u32_e32 v194, s13, v206
	global_load_lds_dwordx4 v194, s[18:19]
	v_add_u32_e32 v194, s13, v213
	s_mov_b32 m0, s40
	s_nop 0
	global_load_lds_dwordx4 v194, s[18:19]
	s_mov_b32 m0, s41
	v_add_u32_e32 v194, 0x90000, v129
	global_load_lds_dwordx4 v194, s[10:11]
	v_add_u32_e32 v194, 0xd8000, v129
	s_mov_b32 m0, s42
	s_nop 0
	global_load_lds_dwordx4 v194, s[10:11]
	s_waitcnt vmcnt(8) lgkmcnt(0)
	s_barrier
	s_setprio 1
	v_mfma_f32_16x16x32_f16 v[12:15], v[130:133], v[146:149], v[12:15]
	v_mfma_f32_16x16x32_f16 v[12:15], v[134:137], v[150:153], v[12:15]
	v_mfma_f32_16x16x32_f16 v[8:11], v[138:141], v[146:149], v[8:11]
	v_mfma_f32_16x16x32_f16 v[8:11], v[142:145], v[150:153], v[8:11]
	v_mfma_f32_16x16x32_f16 v[64:67], v[178:181], v[146:149], v[64:67]
	v_mfma_f32_16x16x32_f16 v[64:67], v[182:185], v[150:153], v[64:67]
	v_mfma_f32_16x16x32_f16 v[68:71], v[186:189], v[146:149], v[68:71]
	v_mfma_f32_16x16x32_f16 v[68:71], v[190:193], v[150:153], v[68:71]
	v_mfma_f32_16x16x32_f16 v[76:79], v[186:189], v[154:157], v[76:79]
	v_mfma_f32_16x16x32_f16 v[76:79], v[190:193], v[158:161], v[76:79]
	v_mfma_f32_16x16x32_f16 v[72:75], v[178:181], v[154:157], v[72:75]
	v_mfma_f32_16x16x32_f16 v[72:75], v[182:185], v[158:161], v[72:75]
	v_mfma_f32_16x16x32_f16 v[0:3], v[138:141], v[154:157], v[0:3]
	v_mfma_f32_16x16x32_f16 v[0:3], v[142:145], v[158:161], v[0:3]
	v_mfma_f32_16x16x32_f16 v[4:7], v[130:133], v[154:157], v[4:7]
	v_mfma_f32_16x16x32_f16 v[4:7], v[134:137], v[158:161], v[4:7]
	v_mfma_f32_16x16x32_f16 v[44:47], v[130:133], v[162:165], v[44:47]
	v_mfma_f32_16x16x32_f16 v[44:47], v[134:137], v[166:169], v[44:47]
	v_mfma_f32_16x16x32_f16 v[48:51], v[138:141], v[162:165], v[48:51]
	v_mfma_f32_16x16x32_f16 v[48:51], v[142:145], v[166:169], v[48:51]
	v_mfma_f32_16x16x32_f16 v[80:83], v[178:181], v[162:165], v[80:83]
	v_mfma_f32_16x16x32_f16 v[80:83], v[182:185], v[166:169], v[80:83]
	v_mfma_f32_16x16x32_f16 v[84:87], v[186:189], v[162:165], v[84:87]
	v_mfma_f32_16x16x32_f16 v[84:87], v[190:193], v[166:169], v[84:87]
	v_mfma_f32_16x16x32_f16 v[92:95], v[186:189], v[170:173], v[92:95]
	v_mfma_f32_16x16x32_f16 v[92:95], v[190:193], v[174:177], v[92:95]
	v_mfma_f32_16x16x32_f16 v[88:91], v[178:181], v[170:173], v[88:91]
	v_mfma_f32_16x16x32_f16 v[88:91], v[182:185], v[174:177], v[88:91]
	v_mfma_f32_16x16x32_f16 v[60:63], v[138:141], v[170:173], v[60:63]
	v_mfma_f32_16x16x32_f16 v[60:63], v[142:145], v[174:177], v[60:63]
	v_mfma_f32_16x16x32_f16 v[56:59], v[130:133], v[170:173], v[56:59]
	v_mfma_f32_16x16x32_f16 v[56:59], v[134:137], v[174:177], v[56:59]
	s_setprio 0
	s_addk_i32 s7, 0x100
	s_cmp_lt_u32 s8, 32
	s_mov_b32 s8, s9
	s_barrier
	s_cbranch_scc1 .LBB1_82
	ds_read_b128 v[132:135], v219 offset:32768
	ds_read_b128 v[136:139], v219 offset:33792
	ds_read_b128 v[140:143], v219 offset:34816
	ds_read_b128 v[144:147], v219 offset:35840
	ds_read_b128 v[128:131], v220
	ds_read_b128 v[148:151], v220 offset:1024
	ds_read_b128 v[152:155], v221
	ds_read_b128 v[156:159], v221 offset:1024
	ds_read_b128 v[188:191], v222
	ds_read_b128 v[192:195], v222 offset:1024
	ds_read_b128 v[196:199], v223
	ds_read_b128 v[200:203], v223 offset:1024
	s_setprio 2
	s_lshl_b32 s3, s50, 9
	s_add_i32 s3, s47, s3
	s_add_i32 s3, s3, 0x10380
	s_mov_b32 m0, s43
	v_add_u32_e32 v160, s3, v206
	global_load_lds_dwordx4 v160, s[18:19]
	v_add_u32_e32 v160, s3, v213
	s_mov_b32 m0, s44
	s_nop 0
	global_load_lds_dwordx4 v160, s[18:19]
	s_setprio 0
	s_waitcnt vmcnt(8)
	s_waitcnt lgkmcnt(0)
	s_barrier
	s_waitcnt lgkmcnt(0)
	s_setprio 1
	s_waitcnt lgkmcnt(0)
	v_mfma_f32_16x16x32_f16 v[124:127], v[132:135], v[128:131], v[124:127]
	v_mfma_f32_16x16x32_f16 v[120:123], v[140:143], v[128:131], v[120:123]
	v_mfma_f32_16x16x32_f16 v[116:119], v[132:135], v[152:155], v[116:119]
	v_mfma_f32_16x16x32_f16 v[112:115], v[140:143], v[152:155], v[112:115]
	v_mfma_f32_16x16x32_f16 v[108:111], v[132:135], v[188:191], v[108:111]
	v_mfma_f32_16x16x32_f16 v[104:107], v[140:143], v[188:191], v[104:107]
	v_mfma_f32_16x16x32_f16 v[100:103], v[132:135], v[196:199], v[100:103]
	v_mfma_f32_16x16x32_f16 v[96:99], v[140:143], v[196:199], v[96:99]
	v_mfma_f32_16x16x32_f16 v[160:163], v[136:139], v[148:151], v[124:127]
	v_mfma_f32_16x16x32_f16 v[164:167], v[144:147], v[148:151], v[120:123]
	v_mfma_f32_16x16x32_f16 v[168:171], v[136:139], v[156:159], v[116:119]
	v_mfma_f32_16x16x32_f16 v[172:175], v[144:147], v[156:159], v[112:115]
	v_mfma_f32_16x16x32_f16 v[176:179], v[136:139], v[192:195], v[108:111]
	v_mfma_f32_16x16x32_f16 v[180:183], v[144:147], v[192:195], v[104:107]
	v_mfma_f32_16x16x32_f16 v[100:103], v[136:139], v[200:203], v[100:103]
	v_mfma_f32_16x16x32_f16 v[184:187], v[144:147], v[200:203], v[96:99]
	s_setprio 0
	s_barrier
	ds_read_b128 v[104:107], v219 offset:49152
	ds_read_b128 v[108:111], v219 offset:50176
	ds_read_b128 v[116:119], v219 offset:51200
	ds_read_b128 v[236:239], v219 offset:52224
	s_waitcnt lgkmcnt(0)
	s_barrier
	s_waitcnt lgkmcnt(0)
	s_setprio 1
	s_waitcnt lgkmcnt(0)
	v_mfma_f32_16x16x32_f16 v[52:55], v[104:107], v[128:131], v[52:55]
	v_mfma_f32_16x16x32_f16 v[40:43], v[116:119], v[128:131], v[40:43]
	v_mfma_f32_16x16x32_f16 v[36:39], v[104:107], v[152:155], v[36:39]
	v_mfma_f32_16x16x32_f16 v[32:35], v[116:119], v[152:155], v[32:35]
	v_mfma_f32_16x16x32_f16 v[28:31], v[104:107], v[188:191], v[28:31]
	v_mfma_f32_16x16x32_f16 v[24:27], v[116:119], v[188:191], v[24:27]
	v_mfma_f32_16x16x32_f16 v[20:23], v[104:107], v[196:199], v[20:23]
	v_mfma_f32_16x16x32_f16 v[16:19], v[116:119], v[196:199], v[16:19]
	v_mfma_f32_16x16x32_f16 v[52:55], v[108:111], v[148:151], v[52:55]
	v_mfma_f32_16x16x32_f16 v[40:43], v[236:239], v[148:151], v[40:43]
	v_mfma_f32_16x16x32_f16 v[36:39], v[108:111], v[156:159], v[36:39]
	v_mfma_f32_16x16x32_f16 v[32:35], v[236:239], v[156:159], v[32:35]
	v_mfma_f32_16x16x32_f16 v[28:31], v[108:111], v[192:195], v[28:31]
	v_mfma_f32_16x16x32_f16 v[24:27], v[236:239], v[192:195], v[24:27]
	v_mfma_f32_16x16x32_f16 v[96:99], v[108:111], v[200:203], v[20:23]
	v_mfma_f32_16x16x32_f16 v[16:19], v[236:239], v[200:203], v[16:19]
	s_setprio 0
	s_barrier
	ds_read_b128 v[20:23], v220 offset:16384
	ds_read_b128 v[148:151], v220 offset:17408
	ds_read_b128 v[152:155], v221 offset:16384
	ds_read_b128 v[156:159], v221 offset:17408
	ds_read_b128 v[188:191], v222 offset:16384
	ds_read_b128 v[192:195], v222 offset:17408
	ds_read_b128 v[196:199], v223 offset:16384
	ds_read_b128 v[200:203], v223 offset:17408
	s_waitcnt vmcnt(4)
	s_waitcnt lgkmcnt(0)
	s_barrier
	s_waitcnt lgkmcnt(0)
	s_setprio 1
	s_waitcnt lgkmcnt(0)
	v_mfma_f32_16x16x32_f16 v[0:3], v[140:143], v[152:155], v[0:3]
	v_mfma_f32_16x16x32_f16 v[124:127], v[144:147], v[156:159], v[0:3]
	v_mfma_f32_16x16x32_f16 v[0:3], v[132:135], v[188:191], v[44:47]
	v_mfma_f32_16x16x32_f16 v[128:131], v[136:139], v[192:195], v[0:3]
	v_mfma_f32_16x16x32_f16 v[0:3], v[140:143], v[188:191], v[48:51]
	v_mfma_f32_16x16x32_f16 v[48:51], v[144:147], v[192:195], v[0:3]
	v_mfma_f32_16x16x32_f16 v[0:3], v[132:135], v[196:199], v[56:59]
	v_mfma_f32_16x16x32_f16 v[12:15], v[132:135], v[20:23], v[12:15]
	v_mfma_f32_16x16x32_f16 v[8:11], v[140:143], v[20:23], v[8:11]
	v_mfma_f32_16x16x32_f16 v[4:7], v[132:135], v[152:155], v[4:7]
	v_mfma_f32_16x16x32_f16 v[56:59], v[136:139], v[200:203], v[0:3]
	v_mfma_f32_16x16x32_f16 v[0:3], v[140:143], v[196:199], v[60:63]
	v_mfma_f32_16x16x32_f16 v[112:115], v[136:139], v[148:151], v[12:15]
	v_mfma_f32_16x16x32_f16 v[8:11], v[144:147], v[148:151], v[8:11]
	v_mfma_f32_16x16x32_f16 v[120:123], v[136:139], v[156:159], v[4:7]
	v_mfma_f32_16x16x32_f16 v[60:63], v[144:147], v[200:203], v[0:3]
	s_setprio 0
	s_setprio 1
	v_mfma_f32_16x16x32_f16 v[0:3], v[104:107], v[20:23], v[64:67]
	v_mfma_f32_16x16x32_f16 v[132:135], v[108:111], v[148:151], v[0:3]
	v_mfma_f32_16x16x32_f16 v[0:3], v[116:119], v[20:23], v[68:71]
	v_mfma_f32_16x16x32_f16 v[136:139], v[236:239], v[148:151], v[0:3]
	v_mfma_f32_16x16x32_f16 v[0:3], v[104:107], v[152:155], v[72:75]
	v_mfma_f32_16x16x32_f16 v[140:143], v[108:111], v[156:159], v[0:3]
	v_mfma_f32_16x16x32_f16 v[0:3], v[116:119], v[152:155], v[76:79]
	v_mfma_f32_16x16x32_f16 v[144:147], v[236:239], v[156:159], v[0:3]
	v_mfma_f32_16x16x32_f16 v[0:3], v[104:107], v[188:191], v[80:83]
	v_mfma_f32_16x16x32_f16 v[80:83], v[108:111], v[192:195], v[0:3]
	v_mfma_f32_16x16x32_f16 v[0:3], v[116:119], v[188:191], v[84:87]
	v_mfma_f32_16x16x32_f16 v[148:151], v[236:239], v[192:195], v[0:3]
	v_mfma_f32_16x16x32_f16 v[0:3], v[104:107], v[196:199], v[88:91]
	v_mfma_f32_16x16x32_f16 v[152:155], v[108:111], v[200:203], v[0:3]
	v_mfma_f32_16x16x32_f16 v[0:3], v[116:119], v[196:199], v[92:95]
	v_mfma_f32_16x16x32_f16 v[156:159], v[236:239], v[200:203], v[0:3]
	s_setprio 0
	s_add_i32 s49, s49, s17
	s_cmpk_lt_i32 s49, 0x1c8
	s_cselect_b64 s[6:7], -1, 0
	s_cmpk_gt_i32 s49, 0x1c7
	s_cselect_b64 s[12:13], -1, 0
	s_and_b64 vcc, exec, s[12:13]
	s_mov_b32 s54, s2
	s_mov_b32 s53, s51
	s_mov_b32 s55, s52
	s_barrier
	s_cbranch_vccnz .LBB1_100
	s_cmpk_lt_i32 s49, 0x148
	s_cbranch_scc1 .LBB1_88
	s_cmpk_lt_u32 s49, 0x1a0
	s_cbranch_scc1 .LBB1_89
	s_cmpk_lt_u32 s49, 0x1b8
	s_cbranch_scc1 .LBB1_90
	s_cmpk_lt_u32 s49, 0x1c0
	s_cselect_b32 s47, s45, 0xfffffe40
	s_cselect_b32 s48, 3, 4
	s_mov_b32 s3, 1
	s_cmp_lt_i32 s48, 1
	s_movk_i32 s53, 0x64
	s_cbranch_scc0 .LBB1_91
	s_branch .LBB1_99
